# s14
# speedup vs baseline: 1.0100x; 1.0020x over previous
_Z11prep_kernelPKfS0_PKiS2_S0_S0_S0_S0_S0_S0_Pc:
	s_lshr_b32 s4, s2, 2
	v_lshrrev_b32_e32 v2, 6, v0
	s_and_b32 s4, s4, 0x1ffffffe
	s_load_dwordx4 s[28:31], s[0:1], 0x40
	s_load_dwordx8 s[12:19], s[0:1], 0x0
	s_load_dwordx8 s[20:27], s[0:1], 0x20
	s_load_dwordx2 s[32:33], s[0:1], 0x50
	v_and_b32_e32 v1, 15, v0
	s_and_b32 s3, s2, 7
	v_or_b32_e32 v2, s4, v2
	v_lshl_or_b32 v88, v2, 3, s3
	v_cmp_gt_u32_e64 s[10:11], 14, v1
	v_mul_lo_u32 v7, v88, 14
	v_and_b32_e32 v105, 63, v0
	v_cndmask_b32_e64 v6, 13, v1, s[10:11]
	v_add_u32_e32 v2, v7, v6
	v_mul_u32_u24_e32 v4, 12, v2
	v_lshlrev_b32_e32 v5, 2, v6
	v_cmp_gt_u32_e64 s[8:9], 48, v105
	v_cmp_gt_u32_e64 s[6:7], 14, v105
	v_lshlrev_b32_e32 v118, 1, v0
	v_lshrrev_b32_e32 v104, 4, v0
	v_cndmask_b32_e64 v8, 0, v105, s[8:9]
	v_cndmask_b32_e64 v9, 0, v105, s[6:7]
	v_mad_u32_u24 v8, v88, 48, v8
	v_add_lshl_u32 v9, v7, v9, 2
	v_lshlrev_b32_e32 v8, 2, v8
	s_lshl_b32 s2, s2, 3
	s_and_b32 s2, s2, 0x78
	v_and_b32_e32 v106, 30, v118
	v_or_b32_e32 v107, s2, v104
	v_cmp_gt_u32_e64 s[2:3], 23, v106
	v_or_b32_e32 v10, 1, v106
	v_cmp_gt_u32_e64 s[4:5], 23, v10
	v_lshlrev_b32_e32 v11, 7, v106
	v_lshlrev_b32_e32 v10, 7, v10
	v_cndmask_b32_e64 v11, 0, v11, s[2:3]
	v_cndmask_b32_e64 v10, 0, v10, s[4:5]
	v_or_b32_e32 v11, v11, v107
	v_or_b32_e32 v10, v10, v107
	v_lshlrev_b32_e32 v11, 2, v11
	v_lshlrev_b32_e32 v10, 2, v10
	v_lshlrev_b32_e32 v12, 2, v107
	v_lshlrev_b32_e32 v119, 5, v0
	v_lshlrev_b32_e32 v13, 2, v0
	v_and_b32_e32 v109, 12, v13
	v_and_b32_e32 v91, 0xf80, v119
	v_lshl_or_b32 v91, v109, 2, v91
	v_or_b32_e32 v92, 0x1000, v91
	v_lshlrev_b32_e32 v90, 9, v2
	v_and_b32_e32 v16, 48, v0
	v_or_b32_e32 v90, v90, v16
	v_or_b32_e32 v112, 0x80, v0
	v_or_b32_e32 v111, 0x180, v0
	v_or_b32_e32 v108, 0x280, v0
	v_mov_b32_e32 v87, 0
	v_bfe_u32 v110, v0, 4, 2
	s_movk_i32 s34, 0x60
	v_lshrrev_b32_e32 v136, 1, v0
	v_lshrrev_b32_e32 v18, 3, v0
	v_and_b32_e32 v18, 4, v18
	v_and_b32_e32 v19, 24, v0
	v_and_b32_e32 v20, 2, v136
	v_or3_b32 v18, v18, v19, v20
	v_and_or_b32 v136, v136, s34, v18
	v_mul_u32_u24_e32 v18, 0x110, v109
	v_lshl_add_u32 v136, v136, 1, v18
	v_add_u32_e32 v137, 0x1100, v136
	v_add_u32_e32 v138, 0x2200, v136
	v_lshlrev_b32_e32 v18, 9, v88
	v_and_b32_e32 v19, 0x100, v119
	v_lshlrev_b32_e32 v20, 4, v0
	v_and_b32_e32 v20, 48, v20
	v_or3_b32 v139, v18, v19, v20
	v_and_b32_e32 v19, 8, v118
	v_and_b32_e32 v20, 64, v118
	v_or3_b32 v139, v139, v19, v20
	v_lshlrev_b32_e32 v19, 2, v110
	v_and_b32_e32 v20, 4, v19
	v_or_b32_e32 v139, v139, v20
	v_lshl_or_b32 v140, v1, 5, v18
	v_or_b32_e32 v140, v140, v19
	v_add_u32_e32 v140, 0x80000, v140
	v_lshl_or_b32 v141, v88, 4, v1
	v_lshlrev_b32_e32 v141, 3, v141
	v_add_u32_e32 v141, 0x140000, v141
	v_lshlrev_b32_e32 v20, 8, v88
	v_mul_u32_u24_e32 v21, 43, v105
	v_lshrrev_b32_e32 v21, 9, v21
	v_mul_u32_u24_e32 v21, 12, v21
	v_sub_u32_e32 v22, v105, v21
	v_and_b32_e32 v142, 3, v22
	v_lshrrev_b32_e32 v22, 2, v22
	v_mad_u32_u24 v142, v142, 3, v22
	v_add_u32_e32 v142, v142, v21
	v_lshl_add_u32 v142, v142, 2, v20
	v_add_u32_e32 v142, 0x164000, v142
	v_lshl_add_u32 v143, v105, 2, v20
	v_add_u32_e32 v143, 0x164000, v143
	v_lshlrev_b32_e32 v123, 6, v107
	v_lshl_add_u32 v123, v106, 1, v123
	v_add_u32_e32 v123, 0x160000, v123
	v_lshl_add_u32 v122, v1, 4, v20
	v_or_b32_e32 v122, v122, v19
	v_add_u32_e32 v122, 0x100000, v122
	s_waitcnt lgkmcnt(0)
	global_load_dwordx3 v[82:84], v4, s[12:13]
	global_load_dword v85, v5, s[26:27]
	global_load_dword v114, v8, s[18:19]
	global_load_dword v115, v9, s[16:17]
	global_load_dword v116, v11, s[28:29]
	global_load_dword v113, v10, s[28:29]
	global_load_dword v117, v12, s[30:31]
	global_load_dwordx4 v[66:69], v91, s[20:21]
	global_load_dwordx4 v[70:73], v91, s[20:21] offset:64
	global_load_dwordx4 v[74:77], v92, s[20:21]
	global_load_dwordx4 v[78:81], v92, s[20:21] offset:64
	global_load_dwordx4 v[58:61], v91, s[22:23]
	global_load_dwordx4 v[62:65], v91, s[22:23] offset:64
	global_load_dwordx4 v[50:53], v92, s[22:23]
	global_load_dwordx4 v[54:57], v92, s[22:23] offset:64
	global_load_dwordx4 v[42:45], v91, s[24:25]
	global_load_dwordx4 v[46:49], v91, s[24:25] offset:64
	global_load_dwordx4 v[34:37], v92, s[24:25]
	global_load_dwordx4 v[38:41], v92, s[24:25] offset:64
	global_load_dwordx4 v[26:29], v90, s[14:15] nt
	global_load_dwordx4 v[30:33], v90, s[14:15] offset:64 nt
	global_load_dwordx4 v[18:21], v90, s[14:15] offset:128 nt
	global_load_dwordx4 v[22:25], v90, s[14:15] offset:192 nt
	global_load_dwordx4 v[10:13], v90, s[14:15] offset:256 nt
	global_load_dwordx4 v[14:17], v90, s[14:15] offset:320 nt
	global_load_dwordx4 v[2:5], v90, s[14:15] offset:384 nt
	global_load_dwordx4 v[6:9], v90, s[14:15] offset:448 nt
	s_waitcnt vmcnt(26)
	v_mov_b32_e32 v90, v83
	v_mov_b32_e32 v91, v84
	v_lshlrev_b32_e32 v86, 2, v110
	s_waitcnt vmcnt(25)
	v_mul_f32_e32 v84, 0x3fb8aa3b, v85
	s_mov_b32 s14, 0x41700000
	v_exp_f32_e32 v84, v84
	v_cndmask_b32_e64 v94, 0, 1.0, s[10:11]
	v_add_f32_e32 v84, 1.0, v84
	v_cmp_lt_f32_e32 vcc, s14, v85
	v_log_f32_e32 v84, v84
	v_cmp_lt_u32_e64 s[12:13], 15, v105
	v_mul_f32_e32 v84, 0x3f317218, v84
	v_cndmask_b32_e32 v84, v84, v85, vcc
	v_mul_f32_e32 v84, 0xbe715bef, v84
	v_mul_f32_e32 v84, 0x3f3504f3, v84
	v_mul_f32_e32 v84, 0x41800000, v84
	v_cndmask_b32_e64 v99, 0, v84, s[10:11]
	v_mul_f32_e32 v101, -2.0, v99
	v_mul_f32_e32 v100, v82, v82
	v_cmp_gt_u32_e32 vcc, 16, v105
	v_fmac_f32_e32 v100, v90, v90
	v_cmp_eq_u32_e64 s[12:13], 0, v110
	v_fmac_f32_e32 v100, v91, v91
	v_cmp_eq_u32_e64 s[14:15], 1, v110
	v_mul_f32_e32 v83, v101, v82
	v_cmp_eq_u32_e64 s[16:17], 2, v110
	v_mul_f32_e32 v84, v101, v90
	v_mul_f32_e32 v85, v101, v91
	v_mul_f32_e32 v89, v99, v100
	v_mul_f32_e32 v92, v82, v94
	v_mul_f32_e32 v93, v90, v94
	v_mul_f32_e32 v95, v91, v94
	v_mul_f32_e32 v96, v100, v94
	v_cvt_pk_fp8_f32 v88, v83, v83
	v_cvt_pk_fp8_f32 v104, v84, v84
	v_cvt_f32_fp8_e32 v97, v88
	v_cvt_f32_fp8_e32 v98, v104
	v_sub_f32_e32 v97, v83, v97
	v_sub_f32_e32 v98, v84, v98
	v_cvt_pk_fp8_f32 v88, v85, v85
	v_cvt_pk_fp8_f32 v104, v99, v99
	v_cvt_f32_fp8_e32 v101, v88
	v_cvt_f32_fp8_e32 v102, v104
	v_sub_f32_e32 v101, v85, v101
	v_sub_f32_e32 v102, v99, v102
	v_cvt_pk_fp8_f32 v88, v89, v89
	v_cvt_pk_fp8_f32 v104, v92, v92
	v_cvt_f32_fp8_e32 v103, v88
	v_cvt_f32_fp8_e32 v120, v104
	v_sub_f32_e32 v103, v89, v103
	v_sub_f32_e32 v120, v92, v120
	v_cvt_pk_fp8_f32 v88, v93, v93
	v_cvt_pk_fp8_f32 v104, v95, v95
	v_cvt_f32_fp8_e32 v121, v88
	v_cvt_f32_fp8_e32 v86, v104
	v_sub_f32_e32 v121, v93, v121
	v_sub_f32_e32 v86, v95, v86
	v_cvt_pk_fp8_f32 v88, v96, v96
	s_nop 0
	v_cvt_f32_fp8_e32 v87, v88
	s_nop 0
	v_sub_f32_e32 v87, v96, v87
	v_cndmask_b32_e64 v124, v89, v85, s[16:17]
	v_cndmask_b32_e64 v124, v124, v98, s[14:15]
	v_cndmask_b32_e64 v124, v124, v83, s[12:13]
	v_cndmask_b32_e64 v125, v103, v99, s[16:17]
	v_cndmask_b32_e64 v125, v125, v84, s[14:15]
	v_cndmask_b32_e64 v125, v125, v97, s[12:13]
	v_cndmask_b32_e64 v126, 0, v102, s[16:17]
	v_cndmask_b32_e64 v126, v126, v85, s[14:15]
	v_cndmask_b32_e64 v126, v126, v83, s[12:13]
	v_cndmask_b32_e64 v127, 0, v99, s[16:17]
	v_cndmask_b32_e64 v127, v127, v101, s[14:15]
	v_cndmask_b32_e64 v127, v127, v84, s[12:13]
	v_cndmask_b32_e64 v128, v94, v86, s[16:17]
	v_cndmask_b32_e64 v128, v128, v93, s[14:15]
	v_cndmask_b32_e64 v128, v128, v92, s[12:13]
	v_cndmask_b32_e64 v129, v94, v96, s[16:17]
	v_cndmask_b32_e64 v129, v129, v121, s[14:15]
	v_cndmask_b32_e64 v129, v129, v92, s[12:13]
	v_cndmask_b32_e64 v130, 0, v96, s[16:17]
	v_cndmask_b32_e64 v130, v130, v95, s[14:15]
	v_cndmask_b32_e64 v130, v130, v120, s[12:13]
	v_cndmask_b32_e64 v131, 0, v87, s[16:17]
	v_cndmask_b32_e64 v131, v131, v95, s[14:15]
	v_cndmask_b32_e64 v131, v131, v93, s[12:13]
	v_cvt_pk_fp8_f32 v119, v124, v125
	v_cvt_pk_fp8_f32 v103, v128, v129
	v_cvt_pk_fp8_f32 v119, v126, v127 op_sel:[0,0,1]
	v_cvt_pk_fp8_f32 v103, v130, v131 op_sel:[0,0,1]
	s_nop 0
	global_store_dword v139, v119, s[32:33] offset:128
	global_store_dword v140, v103, s[32:33] offset:16
	s_and_saveexec_b64 s[0:1], vcc
	s_cbranch_execz .LBB0_14
	v_cvt_f16_f32_e32 v83, v82
	v_cvt_pk_f16_f32 v90, v90, v91
	s_nop 0
	v_alignbit_b32 v91, 0, v90, 16
	v_pack_b32_f16 v90, v83, v90
	global_store_dwordx2 v141, v[90:91], s[32:33]
